# in-projection GEMM: column tiles dealt so every workgroup gets one tile of each epilogue type (on top of v12)
# baseline (speedup 1.0000x reference)
.LBB0_290:
	s_or_b64 exec, exec, s[6:7]
	s_mov_b64 s[36:37], s[0:1]
	s_mov_b64 s[38:39], s[0:1]
	s_mov_b64 s[6:7], s[0:1]
	s_mov_b64 s[8:9], s[0:1]
	s_mov_b64 s[12:13], s[0:1]
	s_mov_b64 s[14:15], s[0:1]
	s_mov_b64 s[10:11], s[0:1]
	s_mov_b64 s[16:17], s[0:1]
	s_mov_b64 s[20:21], s[0:1]
	s_mov_b64 s[18:19], s[0:1]
	s_mov_b64 s[22:23], s[0:1]
	s_mov_b64 s[28:29], s[0:1]
	s_mov_b64 s[24:25], s[0:1]
	s_mov_b64 s[30:31], s[0:1]
	s_mov_b64 s[34:35], s[0:1]
	v_mov_b32_e32 v12, v0
	s_cmpk_lt_i32 s2, 0x700
	s_waitcnt lgkmcnt(0)
	s_barrier
	s_cselect_b64 s[40:41], -1, 0
	s_cmpk_gt_i32 s2, 0x6ff
	v_readfirstlane_b32 s60, v12
	s_cbranch_scc1 .LBB0_292
	s_ashr_i32 s3, s2, 31
	s_lshr_b32 s3, s3, 29
	s_add_i32 s3, s2, s3
	s_ashr_i32 s10, s3, 3
	s_and_b32 s3, s3, -8
	s_sub_i32 s3, s2, s3
	s_cmp_lt_i32 s3, 0
	s_movk_i32 s11, 0xe1
	s_cselect_b32 s11, s11, 0xe0
	s_mul_i32 s3, s3, s11
	s_add_i32 s3, s3, s10
	s_mul_hi_i32 s10, s3, 0x92492493
	s_add_i32 s10, s10, s3
	s_lshr_b32 s11, s10, 31
	s_ashr_i32 s10, s10, 8
	s_add_i32 s10, s10, s11
	s_lshl_b32 s11, s10, 3
	s_mulk_i32 s10, 0x1c0
	s_sub_i32 s3, s3, s10
	s_sext_i32_i16 s10, s3
	s_bfe_u32 s10, s10, 0x3001c
	s_add_i32 s10, s3, s10
	s_sext_i32_i16 s42, s10
	s_and_b32 s10, s10, 0xfff8
	s_sub_i32 s3, s3, s10
	s_sext_i32_i16 s3, s3
	s_add_i32 s10, s11, s3
	s_ashr_i32 s64, s42, 3
	s_cmp_ge_i32 s64, 28
	s_cselect_b32 s98, 28, 0
	s_cselect_b32 s99, 1, 0
	s_sub_i32 s64, s64, s98
	s_lshl1_add_u32 s64, s64, s99

.LBB0_298:
	s_add_i32 s91, s91, 1
	s_mul_i32 s8, s91, s39
	s_mul_hi_u32 s9, s91, s38
	s_add_i32 s9, s9, s8
	s_mul_i32 s8, s91, s38
	s_add_u32 s60, s8, s2
	s_addc_u32 s61, s9, s87
	v_cmp_gt_i64_e32 vcc, s[60:61], v[176:177]
	v_cmp_lt_i64_e64 s[8:9], s[60:61], v[174:175]
	s_cbranch_vccnz .LBB0_300
	s_ashr_i32 s11, s60, 31
	s_lshr_b32 s11, s11, 29
	s_add_i32 s11, s60, s11
	s_ashr_i32 s16, s11, 3
	s_and_b32 s11, s11, -8
	s_sub_i32 s11, s60, s11
	s_cmp_lt_i32 s11, 0
	s_cselect_b32 s56, s88, 0xe0
	s_mul_i32 s11, s11, s56
	s_add_i32 s11, s11, s16
	s_mul_hi_i32 s16, s11, 0x92492493
	s_add_i32 s16, s16, s11
	s_lshr_b32 s56, s16, 31
	s_ashr_i32 s16, s16, 8
	s_add_i32 s16, s16, s56
	s_lshl_b32 s57, s16, 3
	s_sub_i32 s56, 32, s57
	s_min_i32 s58, s56, 8
	s_abs_i32 s56, s58
	v_cvt_f32_u32_e32 v2, s56
	s_sub_i32 s60, 0, s56
	s_mulk_i32 s16, 0x1c0
	s_sub_i32 s11, s11, s16
	v_rcp_iflag_f32_e32 v2, v2
	s_abs_i32 s16, s11
	s_xor_b32 s59, s11, s58
	s_ashr_i32 s59, s59, 31
	v_mul_f32_e32 v2, 0x4f7ffffe, v2
	v_cvt_u32_f32_e32 v2, v2
	s_nop 0
	v_readfirstlane_b32 s61, v2
	s_mul_i32 s60, s60, s61
	s_mul_hi_u32 s60, s61, s60
	s_add_i32 s61, s61, s60
	s_mul_hi_u32 s60, s16, s61
	s_mul_i32 s61, s60, s56
	s_sub_i32 s16, s16, s61
	s_add_i32 s62, s60, 1
	s_sub_i32 s61, s16, s56
	s_cmp_ge_u32 s16, s56
	s_cselect_b32 s60, s62, s60
	s_cselect_b32 s16, s61, s16
	s_add_i32 s61, s60, 1
	s_cmp_ge_u32 s16, s56
	s_cselect_b32 s16, s61, s60
	s_xor_b32 s16, s16, s59
	s_sub_i32 s56, s16, s59
	s_mul_i32 s16, s56, s58
	s_sub_i32 s11, s11, s16
	s_add_i32 s58, s57, s11
	s_cmp_ge_i32 s56, 28
	s_cselect_b32 s98, 28, 0
	s_cselect_b32 s99, 1, 0
	s_sub_i32 s56, s56, s98
	s_lshl1_add_u32 s56, s56, s99
